# speedup vs baseline: 1.0007x; 1.0007x over previous
.Lu0_2:
	s_waitcnt lgkmcnt(14)
	v_mfma_f32_32x32x16_f16 v[2:17], v[158:161], v[178:181], v[2:17]
	v_exp_f32_e32 v98, v98
	v_exp_f32_e32 v99, v99
	v_exp_f32_e32 v100, v100
	v_exp_f32_e32 v101, v101
	s_waitcnt lgkmcnt(12)
	v_mfma_f32_32x32x16_f16 v[18:33], v[158:161], v[174:177], v[18:33]
	v_exp_f32_e32 v102, v102
	v_exp_f32_e32 v103, v103
	v_exp_f32_e32 v104, v104
	v_exp_f32_e32 v105, v105
	ds_read_b128 v[58:61], v211 offset:16384
	ds_read_b128 v[114:117], v211 offset:20480
	s_waitcnt lgkmcnt(12)
	v_mfma_f32_32x32x16_f16 v[2:17], v[150:153], v[170:173], v[2:17]
	v_exp_f32_e32 v106, v106
	v_exp_f32_e32 v107, v107
	v_exp_f32_e32 v108, v108
	v_exp_f32_e32 v109, v109
	ds_read_b128 v[182:185], v210 offset:16384
	ds_read_b128 v[174:177], v210 offset:20480
	s_waitcnt lgkmcnt(12)
	v_mfma_f32_32x32x16_f16 v[18:33], v[150:153], v[74:77], v[18:33]
	v_exp_f32_e32 v110, v110
	v_exp_f32_e32 v111, v111
	v_exp_f32_e32 v112, v112
	v_exp_f32_e32 v113, v113
	ds_read_b128 v[178:181], v209 offset:16384
	ds_read_b128 v[166:169], v209 offset:20480
	s_waitcnt lgkmcnt(12)
	v_mfma_f32_32x32x16_f16 v[2:17], v[142:145], v[70:73], v[2:17]
	v_exp_f32_e32 v82, v82
	v_exp_f32_e32 v83, v83
	v_exp_f32_e32 v84, v84
	v_exp_f32_e32 v85, v85
	ds_read_b128 v[170:173], v208 offset:16384
	ds_read_b128 v[162:165], v208 offset:20480
	s_waitcnt lgkmcnt(12)
	v_mfma_f32_32x32x16_f16 v[18:33], v[142:145], v[66:69], v[18:33]
	v_exp_f32_e32 v86, v86
	v_exp_f32_e32 v87, v87
	v_exp_f32_e32 v88, v88
	v_exp_f32_e32 v89, v89
	s_waitcnt lgkmcnt(10)
	v_mfma_f32_32x32x16_f16 v[2:17], v[130:133], v[54:57], v[2:17]
	v_exp_f32_e32 v90, v90
	v_exp_f32_e32 v91, v91
	v_exp_f32_e32 v92, v92
	v_exp_f32_e32 v93, v93
	s_waitcnt lgkmcnt(8)
	v_mfma_f32_32x32x16_f16 v[18:33], v[130:133], v[50:53], v[18:33]
	v_exp_f32_e32 v94, v94
	v_exp_f32_e32 v95, v95
	v_exp_f32_e32 v96, v96
	v_exp_f32_e32 v97, v97
	s_waitcnt vmcnt(2) lgkmcnt(0)
	s_barrier
	s_setprio 0
	s_andn2_b64 vcc, exec, s[26:27]
	s_cbranch_vccnz .Lu0_4
	s_waitcnt lgkmcnt(0)
	v_add_u32_e32 v66, s38, v212
	ds_read_b128 v[50:53], v66 offset:49248
	ds_read_b128 v[54:57], v66 offset:49216
	ds_read_b128 v[62:65], v66 offset:49184
	ds_read_b128 v[66:69], v66 offset:49152
	s_waitcnt lgkmcnt(3)
	v_pk_mul_f32 v[14:15], v[14:15], v[50:51]
	s_waitcnt lgkmcnt(2)
	v_pk_mul_f32 v[10:11], v[10:11], v[54:55]
	s_waitcnt lgkmcnt(1)
	v_pk_mul_f32 v[6:7], v[6:7], v[62:63]
	v_pk_mul_f32 v[16:17], v[16:17], v[52:53]
	v_pk_mul_f32 v[12:13], v[12:13], v[56:57]
	v_pk_mul_f32 v[8:9], v[8:9], v[64:65]
	s_waitcnt lgkmcnt(0)
	v_pk_mul_f32 v[4:5], v[4:5], v[68:69]
	v_pk_mul_f32 v[2:3], v[2:3], v[66:67]
	v_pk_mul_f32 v[30:31], v[30:31], v[50:51]
	v_pk_mul_f32 v[26:27], v[26:27], v[54:55]
	v_pk_mul_f32 v[22:23], v[22:23], v[62:63]
	v_pk_mul_f32 v[32:33], v[32:33], v[52:53]
	v_pk_mul_f32 v[28:29], v[28:29], v[56:57]
	v_pk_mul_f32 v[24:25], v[24:25], v[64:65]
	v_pk_mul_f32 v[20:21], v[20:21], v[68:69]
	v_pk_mul_f32 v[18:19], v[18:19], v[66:67]

.Lu0_5:
	s_waitcnt lgkmcnt(14)
	v_mfma_f32_32x32x16_f16 v[2:17], v[158:161], v[126:129], v[2:17]
	v_exp_f32_e32 v66, v66
	v_exp_f32_e32 v67, v67
	v_exp_f32_e32 v68, v68
	v_exp_f32_e32 v69, v69
	s_waitcnt lgkmcnt(12)
	v_mfma_f32_32x32x16_f16 v[18:33], v[158:161], v[122:125], v[18:33]
	v_exp_f32_e32 v70, v70
	v_exp_f32_e32 v71, v71
	v_exp_f32_e32 v72, v72
	v_exp_f32_e32 v73, v73
	ds_read_b128 v[82:85], v211
	ds_read_b128 v[170:173], v211 offset:4096
	s_waitcnt lgkmcnt(12)
	v_mfma_f32_32x32x16_f16 v[2:17], v[150:153], v[118:121], v[2:17]
	v_exp_f32_e32 v74, v74
	v_exp_f32_e32 v75, v75
	v_exp_f32_e32 v76, v76
	v_exp_f32_e32 v77, v77
	ds_read_b128 v[166:169], v210
	ds_read_b128 v[162:165], v210 offset:4096
	s_waitcnt lgkmcnt(12)
	v_mfma_f32_32x32x16_f16 v[18:33], v[150:153], v[114:117], v[18:33]
	v_exp_f32_e32 v78, v78
	v_exp_f32_e32 v79, v79
	v_exp_f32_e32 v80, v80
	v_exp_f32_e32 v81, v81
	ds_read_b128 v[126:129], v209
	ds_read_b128 v[122:125], v209 offset:4096
	s_waitcnt lgkmcnt(12)
	v_mfma_f32_32x32x16_f16 v[2:17], v[142:145], v[106:109], v[2:17]
	v_exp_f32_e32 v50, v50
	v_exp_f32_e32 v51, v51
	v_exp_f32_e32 v52, v52
	v_exp_f32_e32 v53, v53
	ds_read_b128 v[118:121], v208
	ds_read_b128 v[114:117], v208 offset:4096
	s_waitcnt lgkmcnt(12)
	v_mfma_f32_32x32x16_f16 v[18:33], v[142:145], v[102:105], v[18:33]
	v_exp_f32_e32 v54, v54
	v_exp_f32_e32 v55, v55
	v_exp_f32_e32 v56, v56
	v_exp_f32_e32 v57, v57
	s_waitcnt lgkmcnt(10)
	v_mfma_f32_32x32x16_f16 v[2:17], v[130:133], v[98:101], v[2:17]
	v_exp_f32_e32 v58, v58
	v_exp_f32_e32 v59, v59
	v_exp_f32_e32 v60, v60
	v_exp_f32_e32 v61, v61
	s_waitcnt lgkmcnt(8)
	v_mfma_f32_32x32x16_f16 v[18:33], v[130:133], v[86:89], v[18:33]
	v_exp_f32_e32 v62, v62
	v_exp_f32_e32 v63, v63
	v_exp_f32_e32 v64, v64
	v_exp_f32_e32 v65, v65
	s_waitcnt vmcnt(2) lgkmcnt(0)
	s_barrier
	s_setprio 0
	s_andn2_b64 vcc, exec, s[26:27]
	s_cbranch_vccnz .Lu0_7
	s_waitcnt lgkmcnt(0)
	v_add_u32_e32 v98, s38, v212
	ds_read_b128 v[86:89], v98 offset:49248
	ds_read_b128 v[90:93], v98 offset:49216
	ds_read_b128 v[94:97], v98 offset:49152
	ds_read_b128 v[98:101], v98 offset:49184
	s_waitcnt lgkmcnt(3)
	v_pk_mul_f32 v[16:17], v[16:17], v[88:89]
	v_pk_mul_f32 v[14:15], v[14:15], v[86:87]
	s_waitcnt lgkmcnt(2)
	v_pk_mul_f32 v[12:13], v[12:13], v[92:93]
	v_pk_mul_f32 v[10:11], v[10:11], v[90:91]
	s_waitcnt lgkmcnt(0)
	v_pk_mul_f32 v[8:9], v[8:9], v[100:101]
	v_pk_mul_f32 v[6:7], v[6:7], v[98:99]
	v_pk_mul_f32 v[4:5], v[4:5], v[96:97]
	v_pk_mul_f32 v[2:3], v[2:3], v[94:95]
	v_pk_mul_f32 v[32:33], v[32:33], v[88:89]
	v_pk_mul_f32 v[30:31], v[30:31], v[86:87]
	v_pk_mul_f32 v[28:29], v[28:29], v[92:93]
	v_pk_mul_f32 v[26:27], v[26:27], v[90:91]
	v_pk_mul_f32 v[24:25], v[24:25], v[100:101]
	v_pk_mul_f32 v[22:23], v[22:23], v[98:99]
	v_pk_mul_f32 v[20:21], v[20:21], v[96:97]
	v_pk_mul_f32 v[18:19], v[18:19], v[94:95]

.Lu1_2:
	s_waitcnt lgkmcnt(14)
	v_mfma_f32_32x32x16_f16 v[2:17], v[158:161], v[178:181], v[2:17]
	v_exp_f32_e32 v98, v98
	v_exp_f32_e32 v99, v99
	v_exp_f32_e32 v100, v100
	v_exp_f32_e32 v101, v101
	s_waitcnt lgkmcnt(12)
	v_mfma_f32_32x32x16_f16 v[18:33], v[158:161], v[174:177], v[18:33]
	v_exp_f32_e32 v102, v102
	v_exp_f32_e32 v103, v103
	v_exp_f32_e32 v104, v104
	v_exp_f32_e32 v105, v105
	ds_read_b128 v[58:61], v211 offset:8192
	ds_read_b128 v[114:117], v211 offset:12288
	s_waitcnt lgkmcnt(12)
	v_mfma_f32_32x32x16_f16 v[2:17], v[150:153], v[170:173], v[2:17]
	v_exp_f32_e32 v106, v106
	v_exp_f32_e32 v107, v107
	v_exp_f32_e32 v108, v108
	v_exp_f32_e32 v109, v109
	ds_read_b128 v[182:185], v210 offset:8192
	ds_read_b128 v[174:177], v210 offset:12288
	s_waitcnt lgkmcnt(12)
	v_mfma_f32_32x32x16_f16 v[18:33], v[150:153], v[74:77], v[18:33]
	v_exp_f32_e32 v110, v110
	v_exp_f32_e32 v111, v111
	v_exp_f32_e32 v112, v112
	v_exp_f32_e32 v113, v113
	ds_read_b128 v[178:181], v209 offset:8192
	ds_read_b128 v[166:169], v209 offset:12288
	s_waitcnt lgkmcnt(12)
	v_mfma_f32_32x32x16_f16 v[2:17], v[142:145], v[70:73], v[2:17]
	v_exp_f32_e32 v82, v82
	v_exp_f32_e32 v83, v83
	v_exp_f32_e32 v84, v84
	v_exp_f32_e32 v85, v85
	ds_read_b128 v[170:173], v208 offset:8192
	ds_read_b128 v[162:165], v208 offset:12288
	s_waitcnt lgkmcnt(12)
	v_mfma_f32_32x32x16_f16 v[18:33], v[142:145], v[66:69], v[18:33]
	v_exp_f32_e32 v86, v86
	v_exp_f32_e32 v87, v87
	v_exp_f32_e32 v88, v88
	v_exp_f32_e32 v89, v89
	s_waitcnt lgkmcnt(10)
	v_mfma_f32_32x32x16_f16 v[2:17], v[130:133], v[54:57], v[2:17]
	v_exp_f32_e32 v90, v90
	v_exp_f32_e32 v91, v91
	v_exp_f32_e32 v92, v92
	v_exp_f32_e32 v93, v93
	s_waitcnt lgkmcnt(8)
	v_mfma_f32_32x32x16_f16 v[18:33], v[130:133], v[50:53], v[18:33]
	v_exp_f32_e32 v94, v94
	v_exp_f32_e32 v95, v95
	v_exp_f32_e32 v96, v96
	v_exp_f32_e32 v97, v97
	s_waitcnt vmcnt(2) lgkmcnt(0)
	s_barrier
	s_setprio 0
	s_andn2_b64 vcc, exec, s[26:27]
	s_cbranch_vccnz .Lu1_4
	s_waitcnt lgkmcnt(0)
	v_add_u32_e32 v66, s38, v212
	ds_read_b128 v[50:53], v66 offset:49248
	ds_read_b128 v[54:57], v66 offset:49216
	ds_read_b128 v[62:65], v66 offset:49184
	ds_read_b128 v[66:69], v66 offset:49152
	s_waitcnt lgkmcnt(3)
	v_pk_mul_f32 v[14:15], v[14:15], v[50:51]
	s_waitcnt lgkmcnt(2)
	v_pk_mul_f32 v[10:11], v[10:11], v[54:55]
	s_waitcnt lgkmcnt(1)
	v_pk_mul_f32 v[6:7], v[6:7], v[62:63]
	v_pk_mul_f32 v[16:17], v[16:17], v[52:53]
	v_pk_mul_f32 v[12:13], v[12:13], v[56:57]
	v_pk_mul_f32 v[8:9], v[8:9], v[64:65]
	s_waitcnt lgkmcnt(0)
	v_pk_mul_f32 v[4:5], v[4:5], v[68:69]
	v_pk_mul_f32 v[2:3], v[2:3], v[66:67]
	v_pk_mul_f32 v[30:31], v[30:31], v[50:51]
	v_pk_mul_f32 v[26:27], v[26:27], v[54:55]
	v_pk_mul_f32 v[22:23], v[22:23], v[62:63]
	v_pk_mul_f32 v[32:33], v[32:33], v[52:53]
	v_pk_mul_f32 v[28:29], v[28:29], v[56:57]
	v_pk_mul_f32 v[24:25], v[24:25], v[64:65]
	v_pk_mul_f32 v[20:21], v[20:21], v[68:69]
	v_pk_mul_f32 v[18:19], v[18:19], v[66:67]

.Lu1_5:
	s_waitcnt lgkmcnt(14)
	v_mfma_f32_32x32x16_f16 v[2:17], v[158:161], v[126:129], v[2:17]
	v_exp_f32_e32 v66, v66
	v_exp_f32_e32 v67, v67
	v_exp_f32_e32 v68, v68
	v_exp_f32_e32 v69, v69
	s_waitcnt lgkmcnt(12)
	v_mfma_f32_32x32x16_f16 v[18:33], v[158:161], v[122:125], v[18:33]
	v_exp_f32_e32 v70, v70
	v_exp_f32_e32 v71, v71
	v_exp_f32_e32 v72, v72
	v_exp_f32_e32 v73, v73
	ds_read_b128 v[82:85], v211 offset:16384
	ds_read_b128 v[170:173], v211 offset:20480
	s_waitcnt lgkmcnt(12)
	v_mfma_f32_32x32x16_f16 v[2:17], v[150:153], v[118:121], v[2:17]
	v_exp_f32_e32 v74, v74
	v_exp_f32_e32 v75, v75
	v_exp_f32_e32 v76, v76
	v_exp_f32_e32 v77, v77
	ds_read_b128 v[166:169], v210 offset:16384
	ds_read_b128 v[162:165], v210 offset:20480
	s_waitcnt lgkmcnt(12)
	v_mfma_f32_32x32x16_f16 v[18:33], v[150:153], v[114:117], v[18:33]
	v_exp_f32_e32 v78, v78
	v_exp_f32_e32 v79, v79
	v_exp_f32_e32 v80, v80
	v_exp_f32_e32 v81, v81
	ds_read_b128 v[126:129], v209 offset:16384
	ds_read_b128 v[122:125], v209 offset:20480
	s_waitcnt lgkmcnt(12)
	v_mfma_f32_32x32x16_f16 v[2:17], v[142:145], v[106:109], v[2:17]
	v_exp_f32_e32 v50, v50
	v_exp_f32_e32 v51, v51
	v_exp_f32_e32 v52, v52
	v_exp_f32_e32 v53, v53
	ds_read_b128 v[118:121], v208 offset:16384
	ds_read_b128 v[114:117], v208 offset:20480
	s_waitcnt lgkmcnt(12)
	v_mfma_f32_32x32x16_f16 v[18:33], v[142:145], v[102:105], v[18:33]
	v_exp_f32_e32 v54, v54
	v_exp_f32_e32 v55, v55
	v_exp_f32_e32 v56, v56
	v_exp_f32_e32 v57, v57
	s_waitcnt lgkmcnt(10)
	v_mfma_f32_32x32x16_f16 v[2:17], v[130:133], v[98:101], v[2:17]
	v_exp_f32_e32 v58, v58
	v_exp_f32_e32 v59, v59
	v_exp_f32_e32 v60, v60
	v_exp_f32_e32 v61, v61
	s_waitcnt lgkmcnt(8)
	v_mfma_f32_32x32x16_f16 v[18:33], v[130:133], v[86:89], v[18:33]
	v_exp_f32_e32 v62, v62
	v_exp_f32_e32 v63, v63
	v_exp_f32_e32 v64, v64
	v_exp_f32_e32 v65, v65
	s_waitcnt vmcnt(2) lgkmcnt(0)
	s_barrier
	s_setprio 0
	s_andn2_b64 vcc, exec, s[26:27]
	s_cbranch_vccnz .Lu1_7
	s_waitcnt lgkmcnt(0)
	v_add_u32_e32 v98, s38, v212
	ds_read_b128 v[86:89], v98 offset:49248
	ds_read_b128 v[90:93], v98 offset:49216
	ds_read_b128 v[94:97], v98 offset:49152
	ds_read_b128 v[98:101], v98 offset:49184
	s_waitcnt lgkmcnt(3)
	v_pk_mul_f32 v[16:17], v[16:17], v[88:89]
	v_pk_mul_f32 v[14:15], v[14:15], v[86:87]
	s_waitcnt lgkmcnt(2)
	v_pk_mul_f32 v[12:13], v[12:13], v[92:93]
	v_pk_mul_f32 v[10:11], v[10:11], v[90:91]
	s_waitcnt lgkmcnt(0)
	v_pk_mul_f32 v[8:9], v[8:9], v[100:101]
	v_pk_mul_f32 v[6:7], v[6:7], v[98:99]
	v_pk_mul_f32 v[4:5], v[4:5], v[96:97]
	v_pk_mul_f32 v[2:3], v[2:3], v[94:95]
	v_pk_mul_f32 v[32:33], v[32:33], v[88:89]
	v_pk_mul_f32 v[30:31], v[30:31], v[86:87]
	v_pk_mul_f32 v[28:29], v[28:29], v[92:93]
	v_pk_mul_f32 v[26:27], v[26:27], v[90:91]
	v_pk_mul_f32 v[24:25], v[24:25], v[100:101]
	v_pk_mul_f32 v[22:23], v[22:23], v[98:99]
	v_pk_mul_f32 v[20:21], v[20:21], v[96:97]
	v_pk_mul_f32 v[18:19], v[18:19], v[94:95]

.Lu2_2:
	s_waitcnt lgkmcnt(14)
	v_mfma_f32_32x32x16_f16 v[2:17], v[158:161], v[178:181], v[2:17]
	v_exp_f32_e32 v98, v98
	v_exp_f32_e32 v99, v99
	v_exp_f32_e32 v100, v100
	v_exp_f32_e32 v101, v101
	s_waitcnt lgkmcnt(12)
	v_mfma_f32_32x32x16_f16 v[18:33], v[158:161], v[174:177], v[18:33]
	v_exp_f32_e32 v102, v102
	v_exp_f32_e32 v103, v103
	v_exp_f32_e32 v104, v104
	v_exp_f32_e32 v105, v105
	ds_read_b128 v[58:61], v211
	ds_read_b128 v[114:117], v211 offset:4096
	s_waitcnt lgkmcnt(12)
	v_mfma_f32_32x32x16_f16 v[2:17], v[150:153], v[170:173], v[2:17]
	v_exp_f32_e32 v106, v106
	v_exp_f32_e32 v107, v107
	v_exp_f32_e32 v108, v108
	v_exp_f32_e32 v109, v109
	ds_read_b128 v[182:185], v210
	ds_read_b128 v[174:177], v210 offset:4096
	s_waitcnt lgkmcnt(12)
	v_mfma_f32_32x32x16_f16 v[18:33], v[150:153], v[74:77], v[18:33]
	v_exp_f32_e32 v110, v110
	v_exp_f32_e32 v111, v111
	v_exp_f32_e32 v112, v112
	v_exp_f32_e32 v113, v113
	ds_read_b128 v[178:181], v209
	ds_read_b128 v[166:169], v209 offset:4096
	s_waitcnt lgkmcnt(12)
	v_mfma_f32_32x32x16_f16 v[2:17], v[142:145], v[70:73], v[2:17]
	v_exp_f32_e32 v82, v82
	v_exp_f32_e32 v83, v83
	v_exp_f32_e32 v84, v84
	v_exp_f32_e32 v85, v85
	ds_read_b128 v[170:173], v208
	ds_read_b128 v[162:165], v208 offset:4096
	s_waitcnt lgkmcnt(12)
	v_mfma_f32_32x32x16_f16 v[18:33], v[142:145], v[66:69], v[18:33]
	v_exp_f32_e32 v86, v86
	v_exp_f32_e32 v87, v87
	v_exp_f32_e32 v88, v88
	v_exp_f32_e32 v89, v89
	s_waitcnt lgkmcnt(10)
	v_mfma_f32_32x32x16_f16 v[2:17], v[130:133], v[54:57], v[2:17]
	v_exp_f32_e32 v90, v90
	v_exp_f32_e32 v91, v91
	v_exp_f32_e32 v92, v92
	v_exp_f32_e32 v93, v93
	s_waitcnt lgkmcnt(8)
	v_mfma_f32_32x32x16_f16 v[18:33], v[130:133], v[50:53], v[18:33]
	v_exp_f32_e32 v94, v94
	v_exp_f32_e32 v95, v95
	v_exp_f32_e32 v96, v96
	v_exp_f32_e32 v97, v97
	s_waitcnt vmcnt(2) lgkmcnt(0)
	s_barrier
	s_setprio 0
	s_andn2_b64 vcc, exec, s[26:27]
	s_cbranch_vccnz .Lu2_4
	s_waitcnt lgkmcnt(0)
	v_add_u32_e32 v66, s38, v212
	ds_read_b128 v[50:53], v66 offset:49248
	ds_read_b128 v[54:57], v66 offset:49216
	ds_read_b128 v[62:65], v66 offset:49184
	ds_read_b128 v[66:69], v66 offset:49152
	s_waitcnt lgkmcnt(3)
	v_pk_mul_f32 v[14:15], v[14:15], v[50:51]
	s_waitcnt lgkmcnt(2)
	v_pk_mul_f32 v[10:11], v[10:11], v[54:55]
	s_waitcnt lgkmcnt(1)
	v_pk_mul_f32 v[6:7], v[6:7], v[62:63]
	v_pk_mul_f32 v[16:17], v[16:17], v[52:53]
	v_pk_mul_f32 v[12:13], v[12:13], v[56:57]
	v_pk_mul_f32 v[8:9], v[8:9], v[64:65]
	s_waitcnt lgkmcnt(0)
	v_pk_mul_f32 v[4:5], v[4:5], v[68:69]
	v_pk_mul_f32 v[2:3], v[2:3], v[66:67]
	v_pk_mul_f32 v[30:31], v[30:31], v[50:51]
	v_pk_mul_f32 v[26:27], v[26:27], v[54:55]
	v_pk_mul_f32 v[22:23], v[22:23], v[62:63]
	v_pk_mul_f32 v[32:33], v[32:33], v[52:53]
	v_pk_mul_f32 v[28:29], v[28:29], v[56:57]
	v_pk_mul_f32 v[24:25], v[24:25], v[64:65]
	v_pk_mul_f32 v[20:21], v[20:21], v[68:69]
	v_pk_mul_f32 v[18:19], v[18:19], v[66:67]

.Lu2_5:
	s_waitcnt lgkmcnt(14)
	v_mfma_f32_32x32x16_f16 v[2:17], v[158:161], v[126:129], v[2:17]
	v_exp_f32_e32 v66, v66
	v_exp_f32_e32 v67, v67
	v_exp_f32_e32 v68, v68
	v_exp_f32_e32 v69, v69
	s_waitcnt lgkmcnt(12)
	v_mfma_f32_32x32x16_f16 v[18:33], v[158:161], v[122:125], v[18:33]
	v_exp_f32_e32 v70, v70
	v_exp_f32_e32 v71, v71
	v_exp_f32_e32 v72, v72
	v_exp_f32_e32 v73, v73
	ds_read_b128 v[82:85], v211 offset:8192
	ds_read_b128 v[170:173], v211 offset:12288
	s_waitcnt lgkmcnt(12)
	v_mfma_f32_32x32x16_f16 v[2:17], v[150:153], v[118:121], v[2:17]
	v_exp_f32_e32 v74, v74
	v_exp_f32_e32 v75, v75
	v_exp_f32_e32 v76, v76
	v_exp_f32_e32 v77, v77
	ds_read_b128 v[166:169], v210 offset:8192
	ds_read_b128 v[162:165], v210 offset:12288
	s_waitcnt lgkmcnt(12)
	v_mfma_f32_32x32x16_f16 v[18:33], v[150:153], v[114:117], v[18:33]
	v_exp_f32_e32 v78, v78
	v_exp_f32_e32 v79, v79
	v_exp_f32_e32 v80, v80
	v_exp_f32_e32 v81, v81
	ds_read_b128 v[126:129], v209 offset:8192
	ds_read_b128 v[122:125], v209 offset:12288
	s_waitcnt lgkmcnt(12)
	v_mfma_f32_32x32x16_f16 v[2:17], v[142:145], v[106:109], v[2:17]
	v_exp_f32_e32 v50, v50
	v_exp_f32_e32 v51, v51
	v_exp_f32_e32 v52, v52
	v_exp_f32_e32 v53, v53
	ds_read_b128 v[118:121], v208 offset:8192
	ds_read_b128 v[114:117], v208 offset:12288
	s_waitcnt lgkmcnt(12)
	v_mfma_f32_32x32x16_f16 v[18:33], v[142:145], v[102:105], v[18:33]
	v_exp_f32_e32 v54, v54
	v_exp_f32_e32 v55, v55
	v_exp_f32_e32 v56, v56
	v_exp_f32_e32 v57, v57
	s_waitcnt lgkmcnt(10)
	v_mfma_f32_32x32x16_f16 v[2:17], v[130:133], v[98:101], v[2:17]
	v_exp_f32_e32 v58, v58
	v_exp_f32_e32 v59, v59
	v_exp_f32_e32 v60, v60
	v_exp_f32_e32 v61, v61
	s_waitcnt lgkmcnt(8)
	v_mfma_f32_32x32x16_f16 v[18:33], v[130:133], v[86:89], v[18:33]
	v_exp_f32_e32 v62, v62
	v_exp_f32_e32 v63, v63
	v_exp_f32_e32 v64, v64
	v_exp_f32_e32 v65, v65
	s_waitcnt vmcnt(2) lgkmcnt(0)
	s_barrier
	s_setprio 0
	s_andn2_b64 vcc, exec, s[26:27]
	s_cbranch_vccnz .Lu2_7
	s_waitcnt lgkmcnt(0)
	v_add_u32_e32 v98, s38, v212
	ds_read_b128 v[86:89], v98 offset:49248
	ds_read_b128 v[90:93], v98 offset:49216
	ds_read_b128 v[94:97], v98 offset:49152
	ds_read_b128 v[98:101], v98 offset:49184
	s_waitcnt lgkmcnt(3)
	v_pk_mul_f32 v[16:17], v[16:17], v[88:89]
	v_pk_mul_f32 v[14:15], v[14:15], v[86:87]
	s_waitcnt lgkmcnt(2)
	v_pk_mul_f32 v[12:13], v[12:13], v[92:93]
	v_pk_mul_f32 v[10:11], v[10:11], v[90:91]
	s_waitcnt lgkmcnt(0)
	v_pk_mul_f32 v[8:9], v[8:9], v[100:101]
	v_pk_mul_f32 v[6:7], v[6:7], v[98:99]
	v_pk_mul_f32 v[4:5], v[4:5], v[96:97]
	v_pk_mul_f32 v[2:3], v[2:3], v[94:95]
	v_pk_mul_f32 v[32:33], v[32:33], v[88:89]
	v_pk_mul_f32 v[30:31], v[30:31], v[86:87]
	v_pk_mul_f32 v[28:29], v[28:29], v[92:93]
	v_pk_mul_f32 v[26:27], v[26:27], v[90:91]
	v_pk_mul_f32 v[24:25], v[24:25], v[100:101]
	v_pk_mul_f32 v[22:23], v[22:23], v[98:99]
	v_pk_mul_f32 v[20:21], v[20:21], v[96:97]
	v_pk_mul_f32 v[18:19], v[18:19], v[94:95]
